# speedup vs baseline: 1.0705x; 1.0542x over previous
.LBB3_36:
	s_andn2_b64 vcc, exec, s[6:7]
	s_cbranch_vccnz .LBB3_86
	s_cmpk_gt_u32 s2, 0xff
	s_cbranch_scc1 .LBB3_86
	s_mov_b64 s[40:41], s[0:1]
	s_mov_b32 s44, s18
	s_mov_b32 s45, s19
	s_mov_b32 s46, 0
	s_mov_b32 s60, s2
	s_mov_b32 s49, 0
	s_mov_b32 s47, 0
	s_mov_b32 s48, 0
	s_movk_i32 s50, 0x63
	s_load_dwordx2 s[52:53], s[0:1], 0x30
	s_add_i32 s51, s19, 31
	s_lshr_b32 s51, s51, 5
	s_sub_i32 s51, s51, 0x200
	s_sub_i32 s55, s51, 1
	s_cmp_lt_u32 s55, 0x80
	s_cselect_b32 s51, s51, 0
	v_mov_b32_e32 v248, v0

.LBB3_57:
	s_or_b64 exec, exec, s[4:5]
	s_movk_i32 s4, 0x619
	v_mul_u32_u24_sdwa v3, v0, s4 dst_sel:DWORD dst_unused:UNUSED_PAD src0_sel:WORD_0 src1_sel:DWORD
	v_lshrrev_b32_e32 v3, 16, v3
	v_mul_lo_u16_e32 v4, 42, v3
	v_sub_u16_e32 v6, v0, v4
	s_movk_i32 s4, 0x64
	v_mov_b32_e32 v4, 0x25600
	v_add_u32_e32 v4, s48, v4
	v_mad_u32_u24 v5, v3, s4, v4
	v_mul_u32_u24_e32 v7, 0x619, v51
	v_min_u32_e32 v19, 0x53f, v56
	s_waitcnt lgkmcnt(0)
	s_barrier
	ds_read_b32 v5, v5
	v_lshrrev_b32_e32 v18, 16, v7
	v_mul_u32_u24_e32 v8, 0x619, v19
	v_mad_u32_u24 v7, v18, s4, v4
	v_lshrrev_b32_e32 v20, 16, v8
	v_lshlrev_b16_e32 v6, 3, v6
	v_mad_u32_u24 v4, v20, s4, v4
	ds_read_b32 v7, v7
	ds_read_b32 v21, v4
	v_lshlrev_b32_e32 v190, 1, v6
	v_mul_u32_u24_e32 v3, 0x2b0, v3
	s_mov_b32 s9, 0x15000
	v_add3_u32 v22, v3, v190, s9
	v_mul_lo_u16_e32 v3, 42, v18
	s_movk_i32 s8, 0x2a0
	v_mov_b64_e32 v[12:13], s[10:11]
	v_sub_u16_e32 v3, v51, v3
	s_waitcnt lgkmcnt(2)
	v_mad_i64_i32 v[4:5], s[4:5], v5, s8, v[12:13]
	v_mov_b32_e32 v191, 0
	v_lshlrev_b16_e32 v3, 3, v3
	v_lshl_add_u64 v[14:15], v[4:5], 0, v[190:191]
	s_waitcnt lgkmcnt(1)
	v_mad_i64_i32 v[4:5], s[4:5], v7, s8, v[12:13]
	v_lshlrev_b32_e32 v190, 1, v3
	v_lshl_add_u64 v[16:17], v[4:5], 0, v[190:191]
	v_mul_u32_u24_e32 v3, 0x2b0, v18
	global_load_dwordx4 v[4:7], v[14:15], off
	global_load_dwordx4 v[8:11], v[16:17], off
	v_add3_u32 v16, v3, v190, s9
	v_mul_lo_u16_e32 v3, 42, v20
	v_sub_u16_e32 v3, v19, v3
	v_lshlrev_b16_e32 v3, 3, v3
	s_waitcnt lgkmcnt(0)
	v_mad_i64_i32 v[12:13], s[4:5], v21, s8, v[12:13]
	v_lshlrev_b32_e32 v190, 1, v3
	v_lshl_add_u64 v[12:13], v[12:13], 0, v[190:191]
	global_load_dwordx4 v[12:15], v[12:13], off
	v_cmp_gt_u32_e32 vcc, 2, v2
	v_mul_u32_u24_e32 v17, 0x2b0, v20
	v_lshlrev_b32_e32 v192, 3, v2
	v_cndmask_b32_e64 v3, 32, 40, vcc
	v_or_b32_e32 v3, v3, v2
	v_add3_u32 v17, v17, v190, s9
	v_lshlrev_b32_e32 v190, 3, v3
	s_waitcnt vmcnt(2)
	ds_write_b128 v22, v[4:7]
	s_waitcnt vmcnt(1)
	ds_write_b128 v16, v[8:11]
	s_waitcnt vmcnt(0)
	ds_write_b128 v17, v[12:15]
	s_and_saveexec_b64 s[4:5], s[6:7]
	s_xor_b64 s[4:5], exec, s[4:5]
	v_lshlrev_b32_e32 v192, 3, v2
	v_lshlrev_b32_e32 v190, 3, v3
	v_mov_b32_e32 v193, v191
	s_or_saveexec_b64 s[4:5], s[4:5]
	v_bfe_u32 v0, v0, 3, 5
	s_xor_b64 exec, exec, s[4:5]
	s_cbranch_execz .LBB3_61
	s_movk_i32 s8, 0x64
	v_mov_b32_e32 v4, 0x25604
	v_add_u32_e32 v4, s48, v4
	v_mad_u32_u24 v4, v0, s8, v4
	ds_read_b32 v6, v4
	s_movk_i32 s8, 0x2a0
	v_mov_b64_e32 v[4:5], s[10:11]
	v_mov_b32_e32 v193, 0
	v_mov_b32_e32 v7, v193
	s_waitcnt lgkmcnt(0)
	v_mad_i64_i32 v[4:5], s[8:9], v6, s8, v[4:5]
	v_lshlrev_b32_e32 v6, 4, v2
	v_lshl_add_u64 v[6:7], v[4:5], 0, v[6:7]
	global_load_dwordx4 v[178:181], v[6:7], off
	global_load_dwordx4 v[174:177], v[6:7], off offset:128
	global_load_dwordx4 v[170:173], v[6:7], off offset:256
	global_load_dwordx4 v[166:169], v[6:7], off offset:384
	v_lshlrev_b32_e32 v2, 4, v3
	v_mov_b32_e32 v3, v193
	v_lshl_add_u64 v[2:3], v[4:5], 0, v[2:3]
	global_load_dwordx4 v[186:189], v[6:7], off offset:512
	global_load_dwordx4 v[182:185], v[2:3], off
	v_mov_b32_e32 v191, v193
.LBB3_61:
	s_or_b64 exec, exec, s[4:5]
	s_movk_i32 s5, 0x2b0
	v_mov_b32_e32 v5, 0x15000
	v_mad_u32_u24 v206, v0, s5, v5
	v_mov_b32_e32 v5, 0x3c00
	v_cmp_eq_u32_e32 vcc, 0, v55
	s_movk_i32 s4, 0xf0
	v_mul_u32_u24_e32 v3, 56, v55
	v_cndmask_b32_e32 v208, 0, v5, vcc
	v_lshlrev_b32_e32 v5, 3, v204
	v_lshl_or_b32 v5, v195, 8, v5
	v_add_u32_e32 v209, 0x26a80, v5
	v_mov_b32_e32 v5, 0x23800
	v_mov_b32_e32 v2, 0x1fc00
	v_mad_u32_u24 v4, v204, s5, v3
	s_mov_b32 s8, 0x15000
	v_mad_u32_u24 v207, v204, s4, v5
	v_lshlrev_b32_e32 v5, 3, v205
	v_lshlrev_b32_e32 v194, 4, v205
	v_mad_u32_u24 v2, v204, s4, v2
	v_add3_u32 v210, v207, v3, v5
	v_add3_u32 v212, v4, v194, s8
	s_movk_i32 s4, 0x64
	v_mov_b32_e32 v4, 0x25600
	v_mad_u32_u24 v214, v0, s4, v4
	v_add_u32_e32 v0, 48, v210
	v_cmp_gt_u32_e64 s[4:5], 32, v1
	v_add_u32_e32 v211, v2, v194
	v_add3_u32 v217, v2, v3, v5
	v_cndmask_b32_e64 v218, v209, v0, s[4:5]
	v_mul_u32_u24_e32 v0, 0x1c0, v195
	v_or_b32_e32 v0, v0, v1
	v_lshlrev_b32_e32 v0, 4, v0
	v_mov_b32_e32 v1, 0
	v_add_u32_e32 v2, 0x1000, v0
	v_mov_b32_e32 v3, v1
	v_lshl_add_u64 v[196:197], s[0:1], 0, v[0:1]
	v_lshl_add_u64 v[198:199], s[0:1], 0, v[2:3]
	v_add_u32_e32 v2, 0x1400, v0
	v_add_u32_e32 v0, 0x1800, v0
	v_add_u32_e32 v213, 0x26280, v50
	v_lshl_add_u32 v215, v54, 4, v50
	v_lshl_add_u64 v[200:201], s[0:1], 0, v[2:3]
	v_lshl_add_u64 v[202:203], s[0:1], 0, v[0:1]
	v_mov_b32_e32 v0, v1
	v_mov_b32_e32 v2, v1
	v_mov_b32_e32 v4, v1
	v_mov_b32_e32 v5, v1
	v_mov_b32_e32 v6, v1
	v_mov_b32_e32 v7, v1
	v_mov_b32_e32 v8, v1
	v_mov_b32_e32 v9, v1
	v_mov_b32_e32 v10, v1
	v_mov_b32_e32 v11, v1
	v_mov_b32_e32 v12, v1
	v_mov_b64_e32 v[80:81], v[14:15]
	v_mov_b64_e32 v[64:65], v[14:15]
	v_mov_b64_e32 v[48:49], v[14:15]
	s_mov_b32 s14, 0
	v_add_u32_e32 v216, v207, v194
	s_mov_b32 s15, 0x5040100
	s_movk_i32 s18, 0x2a0
	v_mov_b64_e32 v[78:79], v[12:13]
	v_mov_b64_e32 v[76:77], v[10:11]
	v_mov_b64_e32 v[74:75], v[8:9]
	v_mov_b64_e32 v[72:73], v[6:7]
	v_mov_b64_e32 v[70:71], v[4:5]
	v_mov_b64_e32 v[68:69], v[2:3]
	v_mov_b64_e32 v[66:67], v[0:1]
	v_mov_b64_e32 v[62:63], v[12:13]
	v_mov_b64_e32 v[60:61], v[10:11]
	v_mov_b64_e32 v[58:59], v[8:9]
	v_mov_b64_e32 v[56:57], v[6:7]
	v_mov_b64_e32 v[54:55], v[4:5]
	v_mov_b64_e32 v[52:53], v[2:3]
	v_mov_b64_e32 v[50:51], v[0:1]
	v_mov_b64_e32 v[46:47], v[12:13]
	v_mov_b64_e32 v[44:45], v[10:11]
	v_mov_b64_e32 v[42:43], v[8:9]
	v_mov_b64_e32 v[40:41], v[6:7]
	v_mov_b64_e32 v[38:39], v[4:5]
	v_mov_b64_e32 v[36:37], v[2:3]
	v_mov_b64_e32 v[34:35], v[0:1]
	v_mov_b32_e32 v13, v1
	v_mov_b32_e32 v14, v1
	v_mov_b32_e32 v15, v1
	v_mov_b32_e32 v16, v1
	v_mov_b32_e32 v17, v1
	v_mov_b32_e32 v18, v1
	v_mov_b32_e32 v19, v1
	v_mov_b32_e32 v20, v1
	v_mov_b32_e32 v21, v1
	v_mov_b32_e32 v22, v1
	v_mov_b32_e32 v23, v1
	v_mov_b32_e32 v24, v1
	v_mov_b32_e32 v25, v1
	v_mov_b32_e32 v26, v1
	v_mov_b32_e32 v27, v1
	v_mov_b32_e32 v28, v1
	v_mov_b32_e32 v29, v1
	v_mov_b32_e32 v30, v1
	s_cmp_eq_u32 s47, 2
	s_cbranch_scc1 .Lgru_restore
	s_waitcnt lgkmcnt(0)
	s_barrier
	s_branch .LBB3_63

.LBB3_63:
	s_cmp_eq_u32 s14, s50
	s_cbranch_scc1 .Lgru_dump
	s_and_saveexec_b64 s[0:1], s[6:7]
	s_xor_b64 s[0:1], exec, s[0:1]
	s_cbranch_execz .LBB3_66
	s_and_b32 s21, s14, 1
	s_mulk_i32 s21, 0x1e00
	v_add_u32_e32 v231, s21, v211
	ds_read_b128 v[166:169], v231
	ds_read_b128 v[170:173], v231 offset:32
	ds_read_b128 v[174:177], v231 offset:64
	ds_read_b128 v[178:181], v231 offset:96
	ds_read_b128 v[182:185], v231 offset:128
	ds_read_b128 v[186:189], v231 offset:160
	ds_read_b128 v[196:199], v231 offset:192
	ds_read_b128 v[232:235], v215
	ds_read_b128 v[236:239], v215 offset:7168
	ds_read_b128 v[240:243], v215 offset:14336
	ds_read_b128 v[244:247], v215 offset:1024
	s_cmp_lt_u32 s14, 2
	s_cbranch_scc1 .LBB3_66
	s_waitcnt vmcnt(6)
	v_exp_f32_e32 v0, v2
	v_exp_f32_e32 v2, v3
	v_exp_f32_e32 v3, v4
	v_exp_f32_e32 v4, v5
	s_waitcnt vmcnt(5)
	v_exp_f32_e32 v5, v6
	v_exp_f32_e32 v6, v7
	v_exp_f32_e32 v7, v8
	v_exp_f32_e32 v8, v9
	s_waitcnt vmcnt(4)
	v_exp_f32_e32 v9, v10
	v_exp_f32_e32 v10, v11
	v_exp_f32_e32 v11, v12
	v_exp_f32_e32 v12, v13
	s_waitcnt vmcnt(3)
	v_exp_f32_e32 v13, v14
	v_add_f32_e32 v0, 1.0, v0
	s_waitcnt vmcnt(2)
	v_exp_f32_e32 v14, v18
	v_exp_f32_e32 v18, v19
	v_exp_f32_e32 v19, v20
	v_exp_f32_e32 v20, v21
	s_waitcnt vmcnt(1)
	v_exp_f32_e32 v21, v22
	v_exp_f32_e32 v22, v23
	v_exp_f32_e32 v23, v24
	v_exp_f32_e32 v24, v25
	s_waitcnt vmcnt(0)
	v_exp_f32_e32 v25, v26
	v_exp_f32_e32 v26, v27
	v_exp_f32_e32 v27, v28
	v_exp_f32_e32 v28, v29
	v_exp_f32_e32 v29, v30
	v_add_f32_e32 v30, 1.0, v2
	v_add_f32_e32 v65, 1.0, v11
	v_rcp_f32_e32 v2, v0
	v_add_f32_e32 v79, 1.0, v12
	v_rcp_f32_e32 v12, v65
	v_add_f32_e32 v31, 1.0, v3
	v_rcp_f32_e32 v3, v30
	v_add_f32_e32 v47, 1.0, v6
	v_add_f32_e32 v80, 1.0, v13
	v_rcp_f32_e32 v13, v79
	v_add_f32_e32 v32, 1.0, v4
	v_add_f32_e32 v48, 1.0, v7
	v_rcp_f32_e32 v4, v31
	v_rcp_f32_e32 v7, v47
	v_fma_f32 v0, v2, v34, v66
	v_add_f32_e32 v81, 1.0, v14
	v_rcp_f32_e32 v14, v80
	v_fma_f32 v66, v12, v44, v76
	v_exp_f32_e32 v0, v0
	v_add_f32_e32 v33, 1.0, v5
	v_add_f32_e32 v49, 1.0, v8
	v_rcp_f32_e32 v5, v32
	v_rcp_f32_e32 v8, v48
	v_fma_f32 v31, v3, v35, v67
	v_exp_f32_e32 v66, v66
	v_fma_f32 v67, v13, v45, v77
	v_exp_f32_e32 v31, v31
	v_rcp_f32_e32 v6, v33
	v_fma_f32 v32, v4, v36, v68
	v_fma_f32 v48, v7, v39, v71
	v_exp_f32_e32 v67, v67
	v_fma_f32 v68, v14, v46, v78
	v_exp_f32_e32 v32, v32
	v_exp_f32_e32 v48, v48
	v_add_f32_e32 v0, 1.0, v0
	v_add_f32_e32 v63, 1.0, v9
	v_rcp_f32_e32 v9, v49
	v_fma_f32 v33, v5, v37, v69
	v_fma_f32 v49, v8, v40, v72
	v_exp_f32_e32 v68, v68
	v_add_f32_e32 v76, 1.0, v66
	v_rcp_f32_e32 v66, v0
	v_exp_f32_e32 v33, v33
	v_exp_f32_e32 v49, v49
	v_add_f32_e32 v31, 1.0, v31
	v_fma_f32 v47, v6, v38, v70
	v_add_f32_e32 v77, 1.0, v67
	v_rcp_f32_e32 v67, v31
	v_add_f32_e32 v219, 1.0, v18
	v_rcp_f32_e32 v18, v81
	v_exp_f32_e32 v47, v47
	v_add_f32_e32 v32, 1.0, v32
	v_add_f32_e32 v48, 1.0, v48
	v_add_f32_e32 v78, 1.0, v68
	v_rcp_f32_e32 v68, v32
	v_rcp_f32_e32 v71, v48
	v_fma_f32 v66, v66, -2.0, 1.0
	v_add_f32_e32 v220, 1.0, v19
	v_rcp_f32_e32 v19, v219
	v_add_f32_e32 v33, 1.0, v33
	v_add_f32_e32 v49, 1.0, v49
	v_add_f32_e32 v64, 1.0, v10
	v_sub_f32_e32 v0, v50, v66
	v_rcp_f32_e32 v10, v63
	v_rcp_f32_e32 v69, v33
	v_rcp_f32_e32 v72, v49
	v_fma_f32 v67, v67, -2.0, 1.0
	v_add_f32_e32 v221, 1.0, v20
	v_rcp_f32_e32 v20, v220
	v_add_f32_e32 v47, 1.0, v47
	v_fma_f32 v50, v18, v0, v66
	v_rcp_f32_e32 v11, v64
	v_sub_f32_e32 v0, v51, v67
	v_fma_f32 v63, v9, v41, v73
	v_rcp_f32_e32 v70, v47
	v_fma_f32 v68, v68, -2.0, 1.0
	v_add_f32_e32 v222, 1.0, v21
	v_rcp_f32_e32 v21, v221
	v_exp_f32_e32 v63, v63
	v_fma_f32 v51, v19, v0, v67
	v_fma_f32 v64, v10, v42, v74
	v_sub_f32_e32 v0, v52, v68
	v_fma_f32 v69, v69, -2.0, 1.0
	v_add_f32_e32 v223, 1.0, v22
	v_rcp_f32_e32 v22, v222
	v_exp_f32_e32 v64, v64
	v_fma_f32 v52, v20, v0, v68
	v_fma_f32 v65, v11, v43, v75
	v_sub_f32_e32 v0, v53, v69
	v_fma_f32 v70, v70, -2.0, 1.0
	v_add_f32_e32 v224, 1.0, v23
	v_rcp_f32_e32 v23, v223
	v_exp_f32_e32 v65, v65
	v_add_f32_e32 v63, 1.0, v63
	v_fma_f32 v53, v21, v0, v69
	v_rcp_f32_e32 v73, v63
	v_sub_f32_e32 v0, v54, v70
	v_fma_f32 v71, v71, -2.0, 1.0
	v_add_f32_e32 v225, 1.0, v24
	v_rcp_f32_e32 v24, v224
	v_add_f32_e32 v64, 1.0, v64
	v_fma_f32 v54, v22, v0, v70
	v_rcp_f32_e32 v74, v64
	v_sub_f32_e32 v0, v55, v71
	v_fma_f32 v72, v72, -2.0, 1.0
	v_add_f32_e32 v226, 1.0, v25
	v_rcp_f32_e32 v25, v225
	v_add_f32_e32 v65, 1.0, v65
	v_fma_f32 v55, v23, v0, v71
	v_rcp_f32_e32 v75, v65
	v_sub_f32_e32 v0, v56, v72
	v_fma_f32 v73, v73, -2.0, 1.0
	v_add_f32_e32 v227, 1.0, v26
	v_rcp_f32_e32 v26, v226
	v_fma_f32 v56, v24, v0, v72
	v_rcp_f32_e32 v76, v76
	v_sub_f32_e32 v0, v57, v73
	v_fma_f32 v74, v74, -2.0, 1.0
	v_add_f32_e32 v228, 1.0, v27
	v_rcp_f32_e32 v27, v227
	v_fma_f32 v57, v25, v0, v73
	v_rcp_f32_e32 v77, v77
	v_sub_f32_e32 v0, v58, v74
	v_fma_f32 v75, v75, -2.0, 1.0
	v_add_f32_e32 v229, 1.0, v28
	v_rcp_f32_e32 v28, v228
	v_fma_f32 v58, v26, v0, v74
	v_rcp_f32_e32 v78, v78
	v_sub_f32_e32 v0, v59, v75
	v_fma_f32 v76, v76, -2.0, 1.0
	v_add_f32_e32 v230, 1.0, v29
	v_rcp_f32_e32 v29, v229
	v_fma_f32 v59, v27, v0, v75
	v_rcp_f32_e32 v30, v230
	v_sub_f32_e32 v0, v60, v76
	v_fma_f32 v77, v77, -2.0, 1.0
	v_fma_f32 v60, v28, v0, v76
	v_fma_f32 v78, v78, -2.0, 1.0
	v_sub_f32_e32 v0, v61, v77
	s_nop 0
	v_fma_f32 v61, v29, v0, v77
	v_sub_f32_e32 v0, v62, v78
	s_nop 0
	v_fma_f32 v62, v30, v0, v78
	v_cvt_pk_f16_f32 v33, v52, v53
	v_cvt_f16_f32_e32 v0, v62
	v_cvt_pk_f16_f32 v32, v50, v51
	v_cvt_pk_f16_f32 v49, v56, v57
	v_cvt_pk_f16_f32 v48, v54, v55
	ds_write2_b64 v210, v[32:33], v[48:49] offset1:2
	v_cvt_pk_f16_f32 v33, v60, v61
	v_cvt_pk_f16_f32 v32, v58, v59
	v_perm_b32 v0, v208, v0, s15
	ds_write_b64 v210, v[32:33] offset:32
	ds_write_b64 v218, v[0:1]

.Lgru_tile_end:
	s_mov_b64 exec, -1
	s_add_i32 s49, s49, 1
	s_mov_b32 s47, 0
	s_mov_b32 s48, 0
	s_movk_i32 s50, 0x63
	s_cmp_lg_u32 s51, 0
	s_cbranch_scc1 .Lgru_sched_split
	s_addk_i32 s44, 0x2000
	s_cmp_lt_i32 s44, s45
	s_cbranch_scc0 .LBB3_86
	s_branch .Lgru_next_tile
.Lgru_sched_split:
	s_cmp_gt_u32 s49, 2
	s_cbranch_scc1 .LBB3_86
	s_add_i32 s44, s60, 0x100
	s_lshl_b32 s44, s44, 5
	s_cmp_eq_u32 s49, 2
	s_cbranch_scc1 .Lgru_sched_j2
	s_cmp_ge_u32 s60, s51
	s_cbranch_scc1 .Lgru_next_tile
	s_add_i32 s44, s60, 0x200
	s_lshl_b32 s44, s44, 5
	s_mov_b32 s47, 1
	s_movk_i32 s50, 14
	s_mov_b32 s54, s60
	s_branch .Lgru_next_tile
.Lgru_sched_j2:
	s_cmp_lt_u32 s60, s51
	s_cbranch_scc1 .Lgru_next_tile
	s_lshl_b32 s55, s51, 1
	s_cmp_ge_u32 s60, s55
	s_cbranch_scc1 .LBB3_86
	s_sub_i32 s54, s60, s51
	s_add_i32 s44, s54, 0x200
	s_lshl_b32 s44, s44, 5
	s_mov_b32 s47, 2
	s_movk_i32 s48, 56
.Lgru_next_tile:
	s_mov_b64 exec, -1
	s_mov_b32 s46, 1
	s_mov_b64 s[0:1], s[40:41]
	s_mov_b32 s18, s44
	s_mov_b32 s19, s45
	v_mov_b32_e32 v0, v248
	v_and_b32_e32 v1, 63, v0
	v_lshrrev_b32_e32 v195, 6, v0
	s_waitcnt lgkmcnt(0)
	s_barrier
	s_branch .Lgru_tile

.Lgru_dump:
	s_lshl_b32 s58, s54, 17
	s_add_u32 s58, s58, 0x1120000
	s_add_u32 s58, s16, s58
	s_addc_u32 s59, s17, 0
	v_lshlrev_b32_e32 v219, 4, v248
	v_readfirstlane_b32 s55, v248
	global_store_dwordx4 v219, v[50:53], s[58:59] sc0 sc1
	v_add_u32_e32 v221, 0x2000, v219
	global_store_dwordx4 v221, v[54:57], s[58:59] sc0 sc1
	v_add_u32_e32 v220, 0x4000, v219
	global_store_dwordx4 v220, v[58:61], s[58:59] sc0 sc1
	v_add_u32_e32 v221, 0x6000, v219
	global_store_dwordx4 v221, v[62:65], s[58:59] sc0 sc1
	s_cmp_lt_u32 s55, 0x100
	s_cbranch_scc1 .Lgru_dump_r3
	v_add_u32_e32 v222, 0x7000, v219
	global_store_dwordx4 v222, v[2:5], s[58:59] sc0 sc1
	v_add_u32_e32 v223, 0x8000, v219
	global_store_dwordx4 v223, v[6:9], s[58:59] sc0 sc1
	v_add_u32_e32 v222, 0x9000, v219
	global_store_dwordx4 v222, v[10:13], s[58:59] sc0 sc1
	v_add_u32_e32 v223, 0xa000, v219
	global_store_dwordx4 v223, v[14:17], s[58:59] sc0 sc1
	v_add_u32_e32 v222, 0xb000, v219
	global_store_dwordx4 v222, v[18:21], s[58:59] sc0 sc1
	v_add_u32_e32 v223, 0xc000, v219
	global_store_dwordx4 v223, v[22:25], s[58:59] sc0 sc1
	v_add_u32_e32 v222, 0xd000, v219
	global_store_dwordx4 v222, v[26:29], s[58:59] sc0 sc1
	v_add_u32_e32 v223, 0xe000, v219
	global_store_dwordx4 v223, v[30:33], s[58:59] sc0 sc1
	v_add_u32_e32 v222, 0xf000, v219
	global_store_dwordx4 v222, v[34:37], s[58:59] sc0 sc1
	v_add_u32_e32 v223, 0x10000, v219
	global_store_dwordx4 v223, v[38:41], s[58:59] sc0 sc1
	v_add_u32_e32 v222, 0x11000, v219
	global_store_dwordx4 v222, v[42:45], s[58:59] sc0 sc1
	v_add_u32_e32 v223, 0x12000, v219
	global_store_dwordx4 v223, v[46:49], s[58:59] sc0 sc1
	v_add_u32_e32 v222, 0x13000, v219
	global_store_dwordx4 v222, v[66:69], s[58:59] sc0 sc1
	v_add_u32_e32 v223, 0x14000, v219
	global_store_dwordx4 v223, v[70:73], s[58:59] sc0 sc1
	v_add_u32_e32 v222, 0x15000, v219
	global_store_dwordx4 v222, v[74:77], s[58:59] sc0 sc1
	v_add_u32_e32 v223, 0x16000, v219
	global_store_dwordx4 v223, v[78:81], s[58:59] sc0 sc1
.Lgru_dump_r3:
	v_add_u32_e32 v220, 0x400, v248
	v_min_u32_e32 v220, 0x59f, v220
	v_lshlrev_b32_e32 v220, 4, v220
	v_add_u32_e32 v221, 0x1fc00, v219
	v_add_u32_e32 v222, 0x1fc00, v220
	ds_read_b128 v[224:227], v221
	ds_read_b128 v[228:231], v221 offset:8192
	ds_read_b128 v[232:235], v222
	v_add_u32_e32 v221, 0x18000, v219
	v_add_u32_e32 v222, 0x1a000, v219
	v_add_u32_e32 v223, 0x18000, v220
	s_waitcnt lgkmcnt(2)
	global_store_dwordx4 v221, v[224:227], s[58:59] sc0 sc1
	s_waitcnt lgkmcnt(1)
	global_store_dwordx4 v222, v[228:231], s[58:59] sc0 sc1
	s_waitcnt lgkmcnt(0)
	global_store_dwordx4 v223, v[232:235], s[58:59] sc0 sc1
	s_waitcnt vmcnt(0)
	s_barrier
	s_cmp_lg_u32 s55, 0
	s_cbranch_scc1 .Lgru_tile_end
	v_mov_b32_e32 v219, s54
	v_mov_b32_e32 v220, 1
	global_store_byte v219, v220, s[52:53] offset:12 sc0 sc1
	s_branch .Lgru_tile_end
.Lgru_restore:
	s_lshl_b32 s58, s54, 17
	s_add_u32 s58, s58, 0x1120000
	s_add_u32 s58, s16, s58
	s_addc_u32 s59, s17, 0
	v_lshlrev_b32_e32 v219, 4, v248
	v_readfirstlane_b32 s55, v248
	s_nop 3
	s_cmp_lg_u32 s55, 0
	s_cbranch_scc1 .Lgru_rs_wait
	s_movk_i32 s56, 0x200
.Lgru_rs_poll:
	v_mov_b32_e32 v220, s54
	global_load_ubyte v220, v220, s[52:53] offset:12 sc0 sc1
	s_waitcnt vmcnt(0)
	v_readfirstlane_b32 s57, v220
	s_nop 3
	s_cmp_lg_u32 s57, 0
	s_cbranch_scc1 .Lgru_rs_polled
	s_sleep 8
	s_sub_i32 s56, s56, 1
	s_cmp_lg_u32 s56, 0
	s_cbranch_scc1 .Lgru_rs_poll
.Lgru_rs_polled:
	v_mov_b32_e32 v220, 0x27300
	s_nop 1
	v_mov_b32_e32 v221, s57
	ds_write_b32 v220, v221
	s_waitcnt lgkmcnt(0)
.Lgru_rs_wait:
	s_barrier
	v_mov_b32_e32 v220, 0x27300
	ds_read_b32 v220, v220
	s_waitcnt lgkmcnt(0)
	v_readfirstlane_b32 s57, v220
	s_nop 3
	s_cmp_eq_u32 s57, 0
	s_cbranch_scc1 .Lgru_rs_fallback
	global_load_dwordx4 v[50:53], v219, s[58:59] sc0 sc1
	v_add_u32_e32 v221, 0x2000, v219
	global_load_dwordx4 v[54:57], v221, s[58:59] sc0 sc1
	v_add_u32_e32 v220, 0x4000, v219
	global_load_dwordx4 v[58:61], v220, s[58:59] sc0 sc1
	v_add_u32_e32 v221, 0x6000, v219
	global_load_dwordx4 v[62:65], v221, s[58:59] sc0 sc1
	s_cmp_lt_u32 s55, 0x100
	s_cbranch_scc1 .Lgru_rs_r3
	v_add_u32_e32 v222, 0x7000, v219
	global_load_dwordx4 v[2:5], v222, s[58:59] sc0 sc1
	v_add_u32_e32 v223, 0x8000, v219
	global_load_dwordx4 v[6:9], v223, s[58:59] sc0 sc1
	v_add_u32_e32 v222, 0x9000, v219
	global_load_dwordx4 v[10:13], v222, s[58:59] sc0 sc1
	v_add_u32_e32 v223, 0xa000, v219
	global_load_dwordx4 v[14:17], v223, s[58:59] sc0 sc1
	v_add_u32_e32 v222, 0xb000, v219
	global_load_dwordx4 v[18:21], v222, s[58:59] sc0 sc1
	v_add_u32_e32 v223, 0xc000, v219
	global_load_dwordx4 v[22:25], v223, s[58:59] sc0 sc1
	v_add_u32_e32 v222, 0xd000, v219
	global_load_dwordx4 v[26:29], v222, s[58:59] sc0 sc1
	v_add_u32_e32 v223, 0xe000, v219
	global_load_dwordx4 v[30:33], v223, s[58:59] sc0 sc1
	v_add_u32_e32 v222, 0xf000, v219
	global_load_dwordx4 v[34:37], v222, s[58:59] sc0 sc1
	v_add_u32_e32 v223, 0x10000, v219
	global_load_dwordx4 v[38:41], v223, s[58:59] sc0 sc1
	v_add_u32_e32 v222, 0x11000, v219
	global_load_dwordx4 v[42:45], v222, s[58:59] sc0 sc1
	v_add_u32_e32 v223, 0x12000, v219
	global_load_dwordx4 v[46:49], v223, s[58:59] sc0 sc1
	v_add_u32_e32 v222, 0x13000, v219
	global_load_dwordx4 v[66:69], v222, s[58:59] sc0 sc1
	v_add_u32_e32 v223, 0x14000, v219
	global_load_dwordx4 v[70:73], v223, s[58:59] sc0 sc1
	v_add_u32_e32 v222, 0x15000, v219
	global_load_dwordx4 v[74:77], v222, s[58:59] sc0 sc1
	v_add_u32_e32 v223, 0x16000, v219
	global_load_dwordx4 v[78:81], v223, s[58:59] sc0 sc1
.Lgru_rs_r3:
	v_add_u32_e32 v220, 0x400, v248
	v_min_u32_e32 v220, 0x59f, v220
	v_lshlrev_b32_e32 v220, 4, v220
	v_add_u32_e32 v221, 0x18000, v219
	v_add_u32_e32 v222, 0x1a000, v219
	v_add_u32_e32 v223, 0x18000, v220
	global_load_dwordx4 v[224:227], v221, s[58:59] sc0 sc1
	global_load_dwordx4 v[228:231], v222, s[58:59] sc0 sc1
	global_load_dwordx4 v[232:235], v223, s[58:59] sc0 sc1
	v_add_u32_e32 v221, 0x1fc00, v219
	v_add_u32_e32 v222, 0x1fc00, v220
	s_waitcnt vmcnt(2)
	ds_write_b128 v221, v[224:227]
	s_waitcnt vmcnt(1)
	ds_write_b128 v221, v[228:231] offset:8192
	s_waitcnt vmcnt(0)
	ds_write_b128 v222, v[232:235]
	s_movk_i32 s14, 14
	s_waitcnt lgkmcnt(0)
	s_barrier
	s_branch .LBB3_63
.Lgru_rs_fallback:
	s_mov_b32 s47, 0
	s_mov_b32 s48, 0
	s_branch .Lgru_next_tile

	.amdhsa_kernel _Z8gru_mfmaPKiPKDF16_PKDv8_DF16_S5_S5_S5_S0_S0_PfPKfS8_S8_S8_S0_
		.amdhsa_group_segment_fixed_size 160640
		.amdhsa_private_segment_fixed_size 0
		.amdhsa_kernarg_size 112
		.amdhsa_user_sgpr_count 2
		.amdhsa_user_sgpr_dispatch_ptr 0
		.amdhsa_user_sgpr_queue_ptr 0
		.amdhsa_user_sgpr_kernarg_segment_ptr 1
		.amdhsa_user_sgpr_dispatch_id 0
		.amdhsa_user_sgpr_kernarg_preload_length 0
		.amdhsa_user_sgpr_kernarg_preload_offset 0
		.amdhsa_user_sgpr_private_segment_size 0
		.amdhsa_uses_dynamic_stack 0
		.amdhsa_enable_private_segment 0
		.amdhsa_system_sgpr_workgroup_id_x 1
		.amdhsa_system_sgpr_workgroup_id_y 0
		.amdhsa_system_sgpr_workgroup_id_z 0
		.amdhsa_system_sgpr_workgroup_info 0
		.amdhsa_system_vgpr_workitem_id 0
		.amdhsa_next_free_vgpr 256
		.amdhsa_next_free_sgpr 96
		.amdhsa_accum_offset 256
		.amdhsa_reserve_vcc 1
		.amdhsa_float_round_mode_32 0
		.amdhsa_float_round_mode_16_64 0
		.amdhsa_float_denorm_mode_32 3
		.amdhsa_float_denorm_mode_16_64 3
		.amdhsa_dx10_clamp 1
		.amdhsa_ieee_mode 1
		.amdhsa_fp16_overflow 0
		.amdhsa_tg_split 0
		.amdhsa_exception_fp_ieee_invalid_op 0
		.amdhsa_exception_fp_denorm_src 0
		.amdhsa_exception_fp_ieee_div_zero 0
		.amdhsa_exception_fp_ieee_overflow 0
		.amdhsa_exception_fp_ieee_underflow 0
		.amdhsa_exception_fp_ieee_inexact 0
		.amdhsa_exception_int_div_zero 0
	.end_amdhsa_kernel

amdhsa.kernels:
  - .agpr_count:     0
    .args:
      - .actual_access:  write_only
        .address_space:  global
        .offset:         0
        .size:           8
        .value_kind:     global_buffer
      - .offset:         8
        .size:           4
        .value_kind:     by_value
      - .offset:         16
        .size:           4
        .value_kind:     hidden_block_count_x
      - .offset:         20
        .size:           4
        .value_kind:     hidden_block_count_y
      - .offset:         24
        .size:           4
        .value_kind:     hidden_block_count_z
      - .offset:         28
        .size:           2
        .value_kind:     hidden_group_size_x
      - .offset:         30
        .size:           2
        .value_kind:     hidden_group_size_y
      - .offset:         32
        .size:           2
        .value_kind:     hidden_group_size_z
      - .offset:         34
        .size:           2
        .value_kind:     hidden_remainder_x
      - .offset:         36
        .size:           2
        .value_kind:     hidden_remainder_y
      - .offset:         38
        .size:           2
        .value_kind:     hidden_remainder_z
      - .offset:         56
        .size:           8
        .value_kind:     hidden_global_offset_x
      - .offset:         64
        .size:           8
        .value_kind:     hidden_global_offset_y
      - .offset:         72
        .size:           8
        .value_kind:     hidden_global_offset_z
      - .offset:         80
        .size:           2
        .value_kind:     hidden_grid_dims
    .group_segment_fixed_size: 0
    .kernarg_segment_align: 8
    .kernarg_segment_size: 272
    .language:       OpenCL C
    .language_version:
      - 2
      - 0
    .max_flat_workgroup_size: 1024
    .name:           _Z11zero_kernelPDv4_fi
    .private_segment_fixed_size: 0
    .sgpr_count:     11
    .sgpr_spill_count: 0
    .symbol:         _Z11zero_kernelPDv4_fi.kd
    .uniform_work_group_size: 1
    .uses_dynamic_stack: false
    .vgpr_count:     6
    .vgpr_spill_count: 0
    .wavefront_size: 64
  - .agpr_count:     0
    .args:
      - .actual_access:  read_only
        .address_space:  global
        .offset:         0
        .size:           8
        .value_kind:     global_buffer
      - .actual_access:  read_only
        .address_space:  global
        .offset:         8
        .size:           8
        .value_kind:     global_buffer
      - .actual_access:  read_only
        .address_space:  global
        .offset:         16
        .size:           8
        .value_kind:     global_buffer
      - .actual_access:  read_only
        .address_space:  global
        .offset:         24
        .size:           8
        .value_kind:     global_buffer
      - .actual_access:  write_only
        .address_space:  global
        .offset:         32
        .size:           8
        .value_kind:     global_buffer
      - .actual_access:  read_only
        .address_space:  global
        .offset:         40
        .size:           8
        .value_kind:     global_buffer
      - .actual_access:  read_only
        .address_space:  global
        .offset:         48
        .size:           8
        .value_kind:     global_buffer
      - .address_space:  global
        .offset:         56
        .size:           8
        .value_kind:     global_buffer
      - .address_space:  global
        .offset:         64
        .size:           8
        .value_kind:     global_buffer
      - .address_space:  global
        .offset:         72
        .size:           8
        .value_kind:     global_buffer
      - .address_space:  global
        .offset:         80
        .size:           8
        .value_kind:     global_buffer
      - .offset:         88
        .size:           4
        .value_kind:     hidden_block_count_x
      - .offset:         92
        .size:           4
        .value_kind:     hidden_block_count_y
      - .offset:         96
        .size:           4
        .value_kind:     hidden_block_count_z
      - .offset:         100
        .size:           2
        .value_kind:     hidden_group_size_x
      - .offset:         102
        .size:           2
        .value_kind:     hidden_group_size_y
      - .offset:         104
        .size:           2
        .value_kind:     hidden_group_size_z
      - .offset:         106
        .size:           2
        .value_kind:     hidden_remainder_x
      - .offset:         108
        .size:           2
        .value_kind:     hidden_remainder_y
      - .offset:         110
        .size:           2
        .value_kind:     hidden_remainder_z
      - .offset:         128
        .size:           8
        .value_kind:     hidden_global_offset_x
      - .offset:         136
        .size:           8
        .value_kind:     hidden_global_offset_y
      - .offset:         144
        .size:           8
        .value_kind:     hidden_global_offset_z
      - .offset:         152
        .size:           2
        .value_kind:     hidden_grid_dims
    .group_segment_fixed_size: 61528
    .kernarg_segment_align: 8
    .kernarg_segment_size: 344
    .language:       OpenCL C
    .language_version:
      - 2
      - 0
    .max_flat_workgroup_size: 640
    .name:           _Z11p_gemm_mfmaPKfPKDv8_DF16_S0_S0_PDF16_PKiS6_PiS7_S7_S7_
    .private_segment_fixed_size: 0
    .sgpr_count:     36
    .sgpr_spill_count: 0
    .symbol:         _Z11p_gemm_mfmaPKfPKDv8_DF16_S0_S0_PDF16_PKiS6_PiS7_S7_S7_.kd
    .uniform_work_group_size: 1
    .uses_dynamic_stack: false
    .vgpr_count:     156
    .vgpr_spill_count: 0
    .wavefront_size: 64
  - .agpr_count:     0
    .args:
      - .actual_access:  read_only
        .address_space:  global
        .offset:         0
        .size:           8
        .value_kind:     global_buffer
      - .actual_access:  read_only
        .address_space:  global
        .offset:         8
        .size:           8
        .value_kind:     global_buffer
      - .actual_access:  read_only
        .address_space:  global
        .offset:         16
        .size:           8
        .value_kind:     global_buffer
      - .actual_access:  read_only
        .address_space:  global
        .offset:         24
        .size:           8
        .value_kind:     global_buffer
      - .actual_access:  read_only
        .address_space:  global
        .offset:         32
        .size:           8
        .value_kind:     global_buffer
      - .actual_access:  read_only
        .address_space:  global
        .offset:         40
        .size:           8
        .value_kind:     global_buffer
      - .actual_access:  read_only
        .address_space:  global
        .offset:         48
        .size:           8
        .value_kind:     global_buffer
      - .actual_access:  write_only
        .address_space:  global
        .offset:         56
        .size:           8
        .value_kind:     global_buffer
      - .actual_access:  write_only
        .address_space:  global
        .offset:         64
        .size:           8
        .value_kind:     global_buffer
      - .actual_access:  write_only
        .address_space:  global
        .offset:         72
        .size:           8
        .value_kind:     global_buffer
      - .actual_access:  write_only
        .address_space:  global
        .offset:         80
        .size:           8
        .value_kind:     global_buffer
      - .actual_access:  read_only
        .address_space:  global
        .offset:         88
        .size:           8
        .value_kind:     global_buffer
      - .actual_access:  write_only
        .address_space:  global
        .offset:         96
        .size:           8
        .value_kind:     global_buffer
      - .actual_access:  read_only
        .address_space:  global
        .offset:         104
        .size:           8
        .value_kind:     global_buffer
      - .actual_access:  read_only
        .address_space:  global
        .offset:         112
        .size:           8
        .value_kind:     global_buffer
      - .actual_access:  write_only
        .address_space:  global
        .offset:         120
        .size:           8
        .value_kind:     global_buffer
      - .actual_access:  read_only
        .address_space:  global
        .offset:         128
        .size:           8
        .value_kind:     global_buffer
      - .address_space:  global
        .offset:         136
        .size:           8
        .value_kind:     global_buffer
      - .address_space:  global
        .offset:         144
        .size:           8
        .value_kind:     global_buffer
      - .address_space:  global
        .offset:         152
        .size:           8
        .value_kind:     global_buffer
      - .address_space:  global
        .offset:         160
        .size:           8
        .value_kind:     global_buffer
      - .address_space:  global
        .offset:         168
        .size:           8
        .value_kind:     global_buffer
      - .offset:         176
        .size:           4
        .value_kind:     hidden_block_count_x
      - .offset:         180
        .size:           4
        .value_kind:     hidden_block_count_y
      - .offset:         184
        .size:           4
        .value_kind:     hidden_block_count_z
      - .offset:         188
        .size:           2
        .value_kind:     hidden_group_size_x
      - .offset:         190
        .size:           2
        .value_kind:     hidden_group_size_y
      - .offset:         192
        .size:           2
        .value_kind:     hidden_group_size_z
      - .offset:         194
        .size:           2
        .value_kind:     hidden_remainder_x
      - .offset:         196
        .size:           2
        .value_kind:     hidden_remainder_y
      - .offset:         198
        .size:           2
        .value_kind:     hidden_remainder_z
      - .offset:         216
        .size:           8
        .value_kind:     hidden_global_offset_x
      - .offset:         224
        .size:           8
        .value_kind:     hidden_global_offset_y
      - .offset:         232
        .size:           8
        .value_kind:     hidden_global_offset_z
      - .offset:         240
        .size:           2
        .value_kind:     hidden_grid_dims
    .group_segment_fixed_size: 1024
    .kernarg_segment_align: 8
    .kernarg_segment_size: 432
    .language:       OpenCL C
    .language_version:
      - 2
      - 0
    .max_flat_workgroup_size: 1024
    .name:           _Z12prep_weightsPKfS0_S0_S0_S0_S0_S0_PDF16_S1_S1_S1_S0_S1_S0_S0_PfPKiPiS5_S5_S5_S5_
    .private_segment_fixed_size: 0
    .sgpr_count:     48
    .sgpr_spill_count: 0
    .symbol:         _Z12prep_weightsPKfS0_S0_S0_S0_S0_S0_PDF16_S1_S1_S1_S0_S1_S0_S0_PfPKiPiS5_S5_S5_S5_.kd
    .uniform_work_group_size: 1
    .uses_dynamic_stack: false
    .vgpr_count:     29
    .vgpr_spill_count: 0
    .wavefront_size: 64
  - .agpr_count:     0
    .args:
      - .actual_access:  read_only
        .address_space:  global
        .offset:         0
        .size:           8
        .value_kind:     global_buffer
      - .actual_access:  read_only
        .address_space:  global
        .offset:         8
        .size:           8
        .value_kind:     global_buffer
      - .actual_access:  read_only
        .address_space:  global
        .offset:         16
        .size:           8
        .value_kind:     global_buffer
      - .actual_access:  read_only
        .address_space:  global
        .offset:         24
        .size:           8
        .value_kind:     global_buffer
      - .actual_access:  read_only
        .address_space:  global
        .offset:         32
        .size:           8
        .value_kind:     global_buffer
      - .actual_access:  read_only
        .address_space:  global
        .offset:         40
        .size:           8
        .value_kind:     global_buffer
      - .actual_access:  read_only
        .address_space:  global
        .offset:         48
        .size:           8
        .value_kind:     global_buffer
      - .actual_access:  read_only
        .address_space:  global
        .offset:         56
        .size:           8
        .value_kind:     global_buffer
      - .actual_access:  write_only
        .address_space:  global
        .offset:         64
        .size:           8
        .value_kind:     global_buffer
      - .actual_access:  read_only
        .address_space:  global
        .offset:         72
        .size:           8
        .value_kind:     global_buffer
      - .actual_access:  read_only
        .address_space:  global
        .offset:         80
        .size:           8
        .value_kind:     global_buffer
      - .actual_access:  read_only
        .address_space:  global
        .offset:         88
        .size:           8
        .value_kind:     global_buffer
      - .actual_access:  read_only
        .address_space:  global
        .offset:         96
        .size:           8
        .value_kind:     global_buffer
      - .actual_access:  read_only
        .address_space:  global
        .offset:         104
        .size:           8
        .value_kind:     global_buffer
    .group_segment_fixed_size: 160640
    .kernarg_segment_align: 8
    .kernarg_segment_size: 112
    .language:       OpenCL C
    .language_version:
      - 2
      - 0
    .max_flat_workgroup_size: 512
    .name:           _Z8gru_mfmaPKiPKDF16_PKDv8_DF16_S5_S5_S5_S0_S0_PfPKfS8_S8_S8_S0_
    .private_segment_fixed_size: 0
    .sgpr_count:     27
    .sgpr_spill_count: 0
    .symbol:         _Z8gru_mfmaPKiPKDF16_PKDv8_DF16_S5_S5_S5_S0_S0_PfPKfS8_S8_S8_S0_.kd
    .uniform_work_group_size: 1
    .uses_dynamic_stack: false
    .vgpr_count:     256
    .vgpr_spill_count: 0
    .wavefront_size: 64
  - .agpr_count:     0
    .args:
      - .actual_access:  read_only
        .address_space:  global
        .offset:         0
        .size:           8
        .value_kind:     global_buffer
      - .actual_access:  read_only
        .address_space:  global
        .offset:         8
        .size:           8
        .value_kind:     global_buffer
      - .actual_access:  read_only
        .address_space:  global
        .offset:         16
        .size:           8
        .value_kind:     global_buffer
      - .actual_access:  read_only
        .address_space:  global
        .offset:         24
        .size:           8
        .value_kind:     global_buffer
      - .actual_access:  read_only
        .address_space:  global
        .offset:         32
        .size:           8
        .value_kind:     global_buffer
      - .actual_access:  read_only
        .address_space:  global
        .offset:         40
        .size:           8
        .value_kind:     global_buffer
      - .actual_access:  read_only
        .address_space:  global
        .offset:         48
        .size:           8
        .value_kind:     global_buffer
      - .actual_access:  read_only
        .address_space:  global
        .offset:         56
        .size:           8
        .value_kind:     global_buffer
      - .actual_access:  write_only
        .address_space:  global
        .offset:         64
        .size:           8
        .value_kind:     global_buffer
    .group_segment_fixed_size: 26624
    .kernarg_segment_align: 8
    .kernarg_segment_size: 72
    .language:       OpenCL C
    .language_version:
      - 2
      - 0
    .max_flat_workgroup_size: 256
    .name:           _Z10gcn_kernelPKiS0_S0_S0_PKfS2_S2_S2_Pf
    .private_segment_fixed_size: 0
    .sgpr_count:     42
    .sgpr_spill_count: 0
    .symbol:         _Z10gcn_kernelPKiS0_S0_S0_PKfS2_S2_S2_Pf.kd
    .uniform_work_group_size: 1
    .uses_dynamic_stack: false
    .vgpr_count:     96
    .vgpr_spill_count: 0
    .wavefront_size: 64
